# start-of-phase stagger halved (role-1 workgroups sleep 7 / 14 instead of 14 / 28): the barrier's per-CU flag hand-off already skews the two workgroups
# baseline (speedup 1.0000x reference)
; __global__ void __launch_bounds__(NTHR, 2) mk_fwd(Params prm) {
;     ...
;     for (int ph = prm.ph_lo; ph < prm.ph_hi; ++ph) {
;         if (PROBE_SP >= 0) pr_t0 = __builtin_amdgcn_s_memrealtime();
;         asm volatile("" : "+s"(c.p));
;         { int t_ = threadIdx.x; asm volatile("" : "+v"(t_)); c.tid = t_; }
.LBB0_13:
	s_mov_b32 s101, 0
	ds_read_b32 v2, v146
	s_waitcnt lgkmcnt(0)
	v_readfirstlane_b32 s7, v2
	s_cmp_eq_u32 s7, 0
	s_cbranch_scc1 .Lstag_done
	s_lshr_b32 s6, 0x10884, s66
	s_bitcmp1_b32 s6, 0
	s_cbranch_scc0 .Lstag_n0
	s_sleep 7
.Lstag_n0:
	s_lshr_b32 s6, 0xd068, s66
	s_bitcmp1_b32 s6, 0
	s_cbranch_scc0 .Lstag_n1
	s_sleep 14
